# lean attention loop, waves 4-7 prioritised for the first 44 of every 64 fragments (was 32)
# speedup vs baseline: 1.0011x; 1.0011x over previous
.Lattn_pl0:
	s_waitcnt lgkmcnt(6)
	v_mfma_f32_16x16x32_bf16 v[64:67], v[160:163], v[96:99], 0
	v_exp_f32_e32 v88, v88
	v_mfma_f32_16x16x32_bf16 v[68:71], v[160:163], v[112:115], 0
	v_exp_f32_e32 v92, v92
	ds_read_b128 v[160:163], v201 offset:20480
	s_add_u32 s16, s22, s10
	s_addc_u32 s17, s23, s11
	s_add_u32 s15, s22, s12
	s_addc_u32 s14, s23, s13
	s_add_u32 s8, s16, 0x3bc00200
	s_addc_u32 s9, s17, 0
	s_add_u32 s6, s15, 0x23a50000
	s_addc_u32 s7, s14, 0
	v_mfma_f32_16x16x32_bf16 v[0:3], v[164:167], v[216:219], v[0:3]
	v_cvt_pk_bf16_f32 v242, v80, v81
	v_mfma_f32_16x16x32_bf16 v[4:7], v[164:167], v[238:241], v[4:7]
	v_exp_f32_e32 v89, v89
	ds_read_b128 v[164:167], v209 offset:8192
	s_waitcnt vmcnt(4)
	ds_write_b128 v225, v[152:155] offset:49152
	s_waitcnt lgkmcnt(7)
	v_mfma_f32_16x16x32_bf16 v[68:71], v[168:171], v[116:119], v[68:71]
	v_exp_f32_e32 v93, v93
	v_mfma_f32_16x16x32_bf16 v[64:67], v[168:171], v[100:103], v[64:67]
	v_cvt_pk_bf16_f32 v243, v82, v83
	ds_read_b128 v[168:171], v202 offset:20480
	ds_write_b128 v226, v[156:159] offset:49152
	v_mfma_f32_16x16x32_bf16 v[12:15], v[172:175], v[238:241], v[12:15]
	v_exp_f32_e32 v90, v90
	v_mfma_f32_16x16x32_bf16 v[8:11], v[172:175], v[216:219], v[8:11]
	v_exp_f32_e32 v94, v94
	ds_read_b128 v[172:175], v209 offset:10240
	ds_write_b64 v227, v[132:133] offset:32768
	s_waitcnt lgkmcnt(9)
	v_mfma_f32_16x16x32_bf16 v[64:67], v[176:179], v[104:107], v[64:67]
	v_cvt_pk_bf16_f32 v204, v84, v85
	v_mfma_f32_16x16x32_bf16 v[68:71], v[176:179], v[120:123], v[68:71]
	v_exp_f32_e32 v91, v91
	ds_read_b128 v[176:179], v203 offset:20480
	ds_write_b64 v228, v[134:135] offset:32768
	v_mfma_f32_16x16x32_bf16 v[16:19], v[180:183], v[216:219], v[16:19]
	v_exp_f32_e32 v95, v95
	v_mfma_f32_16x16x32_bf16 v[20:23], v[180:183], v[238:241], v[20:23]
	v_cvt_pk_bf16_f32 v205, v86, v87
	v_add_f32_e32 v220, v220, v88
	ds_read_b128 v[180:183], v209 offset:12288
	ds_write_b64 v229, v[128:129] offset:32768
	s_waitcnt lgkmcnt(11)
	v_mfma_f32_16x16x32_bf16 v[68:71], v[230:233], v[124:127], v[68:71]
	v_add_f32_e32 v221, v221, v92
	v_add_f32_e32 v220, v220, v89
	v_mfma_f32_16x16x32_bf16 v[64:67], v[230:233], v[108:111], v[64:67]
	v_add_f32_e32 v221, v221, v93
	v_cvt_pk_bf16_f32 v244, v88, v89
	ds_read_b128 v[230:233], v246 offset:20480
	ds_write_b64 v184, v[130:131] offset:32768
	v_mfma_f32_16x16x32_bf16 v[28:31], v[234:237], v[238:241], v[28:31]
	v_cvt_pk_bf16_f32 v245, v90, v91
	v_cvt_pk_bf16_f32 v206, v92, v93
	v_mfma_f32_16x16x32_bf16 v[24:27], v[234:237], v[216:219], v[24:27]
	v_cvt_pk_bf16_f32 v207, v94, v95
	ds_read_b128 v[234:237], v209 offset:14336
	global_load_dwordx4 v[132:135], v198, s[8:9]
	s_waitcnt lgkmcnt(12)
	v_mfma_f32_16x16x32_bf16 v[72:75], v[160:163], v[96:99], 0
	v_add_f32_e32 v220, v220, v90
	v_add_f32_e32 v221, v221, v94
	v_mfma_f32_16x16x32_bf16 v[76:79], v[160:163], v[112:115], 0
	v_add_f32_e32 v220, v220, v91
	v_add_f32_e32 v221, v221, v95
	ds_read_b128 v[160:163], v201 offset:24576
	global_load_dwordx4 v[128:131], v199, s[8:9]
	v_mfma_f32_16x16x32_bf16 v[32:35], v[164:167], v[216:219], v[32:35]
	v_add_f32_e32 v194, v194, v220
	v_add_f32_e32 v195, v195, v221
	v_mfma_f32_16x16x32_bf16 v[36:39], v[164:167], v[238:241], v[36:39]
	v_exp_f32_e32 v64, v64
	ds_read_b128 v[164:167], v210 offset:0
	global_load_dwordx4 v[152:155], v196, s[6:7]
	s_waitcnt lgkmcnt(10)
	v_mfma_f32_16x16x32_bf16 v[76:79], v[168:171], v[116:119], v[76:79]
	v_exp_f32_e32 v68, v68
	v_mfma_f32_16x16x32_bf16 v[72:75], v[168:171], v[100:103], v[72:75]
	v_exp_f32_e32 v65, v65
	ds_read_b128 v[168:171], v202 offset:24576
	global_load_dwordx4 v[156:159], v197, s[6:7]
	v_mfma_f32_16x16x32_bf16 v[44:47], v[172:175], v[238:241], v[44:47]
	v_exp_f32_e32 v69, v69
	v_mfma_f32_16x16x32_bf16 v[40:43], v[172:175], v[216:219], v[40:43]
	v_exp_f32_e32 v66, v66
	ds_read_b128 v[172:175], v210 offset:2048
	s_waitcnt lgkmcnt(8)
	v_mfma_f32_16x16x32_bf16 v[72:75], v[176:179], v[104:107], v[72:75]
	v_exp_f32_e32 v70, v70
	v_mfma_f32_16x16x32_bf16 v[76:79], v[176:179], v[120:123], v[76:79]
	v_exp_f32_e32 v67, v67
	ds_read_b128 v[176:179], v203 offset:24576
	v_mfma_f32_16x16x32_bf16 v[48:51], v[180:183], v[216:219], v[48:51]
	v_exp_f32_e32 v71, v71
	v_mfma_f32_16x16x32_bf16 v[52:55], v[180:183], v[238:241], v[52:55]
	v_add_f32_e32 v220, v64, v65
	ds_read_b128 v[180:183], v210 offset:4096
	s_waitcnt lgkmcnt(6)
	v_mfma_f32_16x16x32_bf16 v[76:79], v[230:233], v[124:127], v[76:79]
	v_add_f32_e32 v221, v68, v69
	v_mfma_f32_16x16x32_bf16 v[72:75], v[230:233], v[108:111], v[72:75]
	v_add_f32_e32 v220, v220, v66
	ds_read_b128 v[230:233], v246 offset:24576
	v_mfma_f32_16x16x32_bf16 v[60:63], v[234:237], v[238:241], v[60:63]
	v_add_f32_e32 v221, v221, v70
	v_add_f32_e32 v220, v220, v67
	v_mfma_f32_16x16x32_bf16 v[56:59], v[234:237], v[216:219], v[56:59]
	v_add_f32_e32 v221, v221, v71
	ds_read_b128 v[234:237], v210 offset:6144
	s_waitcnt lgkmcnt(6)
	v_mfma_f32_16x16x32_bf16 v[80:83], v[160:163], v[96:99], 0
	v_exp_f32_e32 v72, v72
	v_mfma_f32_16x16x32_bf16 v[84:87], v[160:163], v[112:115], 0
	v_exp_f32_e32 v76, v76
	ds_read_b128 v[160:163], v201 offset:28672
	v_mfma_f32_16x16x32_bf16 v[0:3], v[164:167], v[242:245], v[0:3]
	v_exp_f32_e32 v73, v73
	v_mfma_f32_16x16x32_bf16 v[4:7], v[164:167], v[204:207], v[4:7]
	v_exp_f32_e32 v77, v77
	ds_read_b128 v[164:167], v210 offset:8192
	s_waitcnt lgkmcnt(6)
	v_mfma_f32_16x16x32_bf16 v[84:87], v[168:171], v[116:119], v[84:87]
	v_exp_f32_e32 v74, v74
	v_mfma_f32_16x16x32_bf16 v[80:83], v[168:171], v[100:103], v[80:83]
	v_exp_f32_e32 v78, v78
	ds_read_b128 v[168:171], v202 offset:28672
	v_mfma_f32_16x16x32_bf16 v[12:15], v[172:175], v[204:207], v[12:15]
	v_exp_f32_e32 v75, v75
	v_mfma_f32_16x16x32_bf16 v[8:11], v[172:175], v[242:245], v[8:11]
	v_exp_f32_e32 v79, v79
	ds_read_b128 v[172:175], v210 offset:10240
	s_waitcnt lgkmcnt(6)
	v_mfma_f32_16x16x32_bf16 v[80:83], v[176:179], v[104:107], v[80:83]
	v_add_f32_e32 v220, v220, v72
	v_add_f32_e32 v221, v221, v76
	v_mfma_f32_16x16x32_bf16 v[84:87], v[176:179], v[120:123], v[84:87]
	v_add_f32_e32 v220, v220, v73
	ds_read_b128 v[176:179], v203 offset:28672
	v_mfma_f32_16x16x32_bf16 v[16:19], v[180:183], v[242:245], v[16:19]
	v_add_f32_e32 v221, v221, v77
	v_add_f32_e32 v220, v220, v74
	v_mfma_f32_16x16x32_bf16 v[20:23], v[180:183], v[204:207], v[20:23]
	v_add_f32_e32 v221, v221, v78
	ds_read_b128 v[180:183], v210 offset:12288
	s_waitcnt lgkmcnt(6)
	v_mfma_f32_16x16x32_bf16 v[84:87], v[230:233], v[124:127], v[84:87]
	v_add_f32_e32 v220, v220, v75
	v_add_f32_e32 v221, v221, v79
	v_mfma_f32_16x16x32_bf16 v[80:83], v[230:233], v[108:111], v[80:83]
	v_cvt_pk_bf16_f32 v216, v64, v65
	ds_read_b128 v[230:233], v246 offset:28672
	v_mfma_f32_16x16x32_bf16 v[28:31], v[234:237], v[204:207], v[28:31]
	v_cvt_pk_bf16_f32 v217, v66, v67
	v_cvt_pk_bf16_f32 v238, v68, v69
	v_mfma_f32_16x16x32_bf16 v[24:27], v[234:237], v[242:245], v[24:27]
	v_cvt_pk_bf16_f32 v239, v70, v71
	ds_read_b128 v[234:237], v210 offset:14336
	s_waitcnt lgkmcnt(6)
	v_mfma_f32_16x16x32_bf16 v[88:91], v[160:163], v[96:99], 0
	v_exp_f32_e32 v80, v80
	v_mfma_f32_16x16x32_bf16 v[92:95], v[160:163], v[112:115], 0
	v_exp_f32_e32 v84, v84
	ds_read_b128 v[160:163], v201 offset:32768
	v_mfma_f32_16x16x32_bf16 v[32:35], v[164:167], v[242:245], v[32:35]
	v_exp_f32_e32 v81, v81
	v_mfma_f32_16x16x32_bf16 v[36:39], v[164:167], v[204:207], v[36:39]
	v_exp_f32_e32 v85, v85
	ds_read_b128 v[164:167], v209 offset:16384
	s_waitcnt lgkmcnt(6)
	v_mfma_f32_16x16x32_bf16 v[92:95], v[168:171], v[116:119], v[92:95]
	v_exp_f32_e32 v82, v82
	v_mfma_f32_16x16x32_bf16 v[88:91], v[168:171], v[100:103], v[88:91]
	v_exp_f32_e32 v86, v86
	ds_read_b128 v[168:171], v202 offset:32768
	v_mfma_f32_16x16x32_bf16 v[44:47], v[172:175], v[204:207], v[44:47]
	v_exp_f32_e32 v83, v83
	v_mfma_f32_16x16x32_bf16 v[40:43], v[172:175], v[242:245], v[40:43]
	v_exp_f32_e32 v87, v87
	ds_read_b128 v[172:175], v209 offset:18432
	s_waitcnt lgkmcnt(6)
	v_mfma_f32_16x16x32_bf16 v[88:91], v[176:179], v[104:107], v[88:91]
	v_add_f32_e32 v220, v220, v80
	v_add_f32_e32 v221, v221, v84
	v_mfma_f32_16x16x32_bf16 v[92:95], v[176:179], v[120:123], v[92:95]
	v_add_f32_e32 v220, v220, v81
	ds_read_b128 v[176:179], v203 offset:32768
	v_mfma_f32_16x16x32_bf16 v[48:51], v[180:183], v[242:245], v[48:51]
	v_add_f32_e32 v221, v221, v85
	v_add_f32_e32 v220, v220, v82
	v_mfma_f32_16x16x32_bf16 v[52:55], v[180:183], v[204:207], v[52:55]
	v_add_f32_e32 v221, v221, v86
	ds_read_b128 v[180:183], v209 offset:20480
	s_waitcnt lgkmcnt(6)
	v_mfma_f32_16x16x32_bf16 v[92:95], v[230:233], v[124:127], v[92:95]
	v_add_f32_e32 v220, v220, v83
	v_add_f32_e32 v221, v221, v87
	v_mfma_f32_16x16x32_bf16 v[88:91], v[230:233], v[108:111], v[88:91]
	v_cvt_pk_bf16_f32 v218, v72, v73
	ds_read_b128 v[230:233], v246 offset:32768
	v_mfma_f32_16x16x32_bf16 v[60:63], v[234:237], v[204:207], v[60:63]
	v_cvt_pk_bf16_f32 v219, v74, v75
	v_cvt_pk_bf16_f32 v240, v76, v77
	v_mfma_f32_16x16x32_bf16 v[56:59], v[234:237], v[242:245], v[56:59]
	v_cvt_pk_bf16_f32 v241, v78, v79
	ds_read_b128 v[234:237], v209 offset:22528
	s_waitcnt lgkmcnt(6)
	v_mfma_f32_16x16x32_bf16 v[64:67], v[160:163], v[96:99], 0
	v_exp_f32_e32 v88, v88
	v_mfma_f32_16x16x32_bf16 v[68:71], v[160:163], v[112:115], 0
	v_exp_f32_e32 v92, v92
	ds_read_b128 v[160:163], v201 offset:36864
	s_add_u32 s8, s16, 0x3bc00280
	s_addc_u32 s9, s17, 0
	s_add_u32 s6, s15, 0x23a60000
	s_addc_u32 s7, s14, 0
	v_mfma_f32_16x16x32_bf16 v[0:3], v[164:167], v[216:219], v[0:3]
	v_cvt_pk_bf16_f32 v242, v80, v81
	v_mfma_f32_16x16x32_bf16 v[4:7], v[164:167], v[238:241], v[4:7]
	v_exp_f32_e32 v89, v89
	ds_read_b128 v[164:167], v209 offset:24576
	s_waitcnt vmcnt(4)
	ds_write_b128 v225, v[136:139] offset:0
	s_waitcnt lgkmcnt(7)
	v_mfma_f32_16x16x32_bf16 v[68:71], v[168:171], v[116:119], v[68:71]
	v_exp_f32_e32 v93, v93
	v_mfma_f32_16x16x32_bf16 v[64:67], v[168:171], v[100:103], v[64:67]
	v_cvt_pk_bf16_f32 v243, v82, v83
	ds_read_b128 v[168:171], v202 offset:36864
	ds_write_b128 v226, v[140:143] offset:0
	v_mfma_f32_16x16x32_bf16 v[12:15], v[172:175], v[238:241], v[12:15]
	v_exp_f32_e32 v90, v90
	v_mfma_f32_16x16x32_bf16 v[8:11], v[172:175], v[216:219], v[8:11]
	v_exp_f32_e32 v94, v94
	ds_read_b128 v[172:175], v209 offset:26624
	ds_write_b64 v227, v[148:149] offset:49152
	s_waitcnt lgkmcnt(9)
	v_mfma_f32_16x16x32_bf16 v[64:67], v[176:179], v[104:107], v[64:67]
	v_cvt_pk_bf16_f32 v204, v84, v85
	v_mfma_f32_16x16x32_bf16 v[68:71], v[176:179], v[120:123], v[68:71]
	v_exp_f32_e32 v91, v91
	ds_read_b128 v[176:179], v203 offset:36864
	ds_write_b64 v228, v[150:151] offset:49152
	v_mfma_f32_16x16x32_bf16 v[16:19], v[180:183], v[216:219], v[16:19]
	v_exp_f32_e32 v95, v95
	v_mfma_f32_16x16x32_bf16 v[20:23], v[180:183], v[238:241], v[20:23]
	v_cvt_pk_bf16_f32 v205, v86, v87
	v_add_f32_e32 v220, v220, v88
	ds_read_b128 v[180:183], v209 offset:28672
	ds_write_b64 v229, v[144:145] offset:49152
	s_waitcnt lgkmcnt(11)
	v_mfma_f32_16x16x32_bf16 v[68:71], v[230:233], v[124:127], v[68:71]
	v_add_f32_e32 v221, v221, v92
	v_add_f32_e32 v220, v220, v89
	v_mfma_f32_16x16x32_bf16 v[64:67], v[230:233], v[108:111], v[64:67]
	v_add_f32_e32 v221, v221, v93
	v_cvt_pk_bf16_f32 v244, v88, v89
	ds_read_b128 v[230:233], v246 offset:36864
	ds_write_b64 v184, v[146:147] offset:49152
	v_mfma_f32_16x16x32_bf16 v[28:31], v[234:237], v[238:241], v[28:31]
	v_cvt_pk_bf16_f32 v245, v90, v91
	v_cvt_pk_bf16_f32 v206, v92, v93
	v_mfma_f32_16x16x32_bf16 v[24:27], v[234:237], v[216:219], v[24:27]
	v_cvt_pk_bf16_f32 v207, v94, v95
	ds_read_b128 v[234:237], v209 offset:30720
	global_load_dwordx4 v[148:151], v198, s[8:9]
	s_waitcnt lgkmcnt(12)
	v_mfma_f32_16x16x32_bf16 v[72:75], v[160:163], v[96:99], 0
	v_add_f32_e32 v220, v220, v90
	v_add_f32_e32 v221, v221, v94
	v_mfma_f32_16x16x32_bf16 v[76:79], v[160:163], v[112:115], 0
	v_add_f32_e32 v220, v220, v91
	v_add_f32_e32 v221, v221, v95
	ds_read_b128 v[160:163], v201 offset:40960
	global_load_dwordx4 v[144:147], v199, s[8:9]
	v_mfma_f32_16x16x32_bf16 v[32:35], v[164:167], v[216:219], v[32:35]
	v_add_f32_e32 v194, v194, v220
	v_add_f32_e32 v195, v195, v221
	v_mfma_f32_16x16x32_bf16 v[36:39], v[164:167], v[238:241], v[36:39]
	v_exp_f32_e32 v64, v64
	ds_read_b128 v[164:167], v210 offset:16384
	global_load_dwordx4 v[136:139], v196, s[6:7]
	s_waitcnt lgkmcnt(10)
	v_mfma_f32_16x16x32_bf16 v[76:79], v[168:171], v[116:119], v[76:79]
	v_exp_f32_e32 v68, v68
	v_mfma_f32_16x16x32_bf16 v[72:75], v[168:171], v[100:103], v[72:75]
	v_exp_f32_e32 v65, v65
	ds_read_b128 v[168:171], v202 offset:40960
	global_load_dwordx4 v[140:143], v197, s[6:7]
	v_mfma_f32_16x16x32_bf16 v[44:47], v[172:175], v[238:241], v[44:47]
	v_exp_f32_e32 v69, v69
	v_mfma_f32_16x16x32_bf16 v[40:43], v[172:175], v[216:219], v[40:43]
	v_exp_f32_e32 v66, v66
	ds_read_b128 v[172:175], v210 offset:18432
	s_setprio 0
	s_waitcnt lgkmcnt(8)
	v_mfma_f32_16x16x32_bf16 v[72:75], v[176:179], v[104:107], v[72:75]
	v_exp_f32_e32 v70, v70
	v_mfma_f32_16x16x32_bf16 v[76:79], v[176:179], v[120:123], v[76:79]
	v_exp_f32_e32 v67, v67
	ds_read_b128 v[176:179], v203 offset:40960
	v_mfma_f32_16x16x32_bf16 v[48:51], v[180:183], v[216:219], v[48:51]
	v_exp_f32_e32 v71, v71
	v_mfma_f32_16x16x32_bf16 v[52:55], v[180:183], v[238:241], v[52:55]
	v_add_f32_e32 v220, v64, v65
	ds_read_b128 v[180:183], v210 offset:20480
	s_waitcnt lgkmcnt(6)
	v_mfma_f32_16x16x32_bf16 v[76:79], v[230:233], v[124:127], v[76:79]
	v_add_f32_e32 v221, v68, v69
	v_mfma_f32_16x16x32_bf16 v[72:75], v[230:233], v[108:111], v[72:75]
	v_add_f32_e32 v220, v220, v66
	ds_read_b128 v[230:233], v246 offset:40960
	v_mfma_f32_16x16x32_bf16 v[60:63], v[234:237], v[238:241], v[60:63]
	v_add_f32_e32 v221, v221, v70
	v_add_f32_e32 v220, v220, v67
	v_mfma_f32_16x16x32_bf16 v[56:59], v[234:237], v[216:219], v[56:59]
	v_add_f32_e32 v221, v221, v71
	ds_read_b128 v[234:237], v210 offset:22528
	s_waitcnt lgkmcnt(6)
	v_mfma_f32_16x16x32_bf16 v[80:83], v[160:163], v[96:99], 0
	v_exp_f32_e32 v72, v72
	v_mfma_f32_16x16x32_bf16 v[84:87], v[160:163], v[112:115], 0
	v_exp_f32_e32 v76, v76
	ds_read_b128 v[160:163], v201 offset:45056
	v_mfma_f32_16x16x32_bf16 v[0:3], v[164:167], v[242:245], v[0:3]
	v_exp_f32_e32 v73, v73
	v_mfma_f32_16x16x32_bf16 v[4:7], v[164:167], v[204:207], v[4:7]
	v_exp_f32_e32 v77, v77
	ds_read_b128 v[164:167], v210 offset:24576
	s_waitcnt lgkmcnt(6)
	v_mfma_f32_16x16x32_bf16 v[84:87], v[168:171], v[116:119], v[84:87]
	v_exp_f32_e32 v74, v74
	v_mfma_f32_16x16x32_bf16 v[80:83], v[168:171], v[100:103], v[80:83]
	v_exp_f32_e32 v78, v78
	ds_read_b128 v[168:171], v202 offset:45056
	v_mfma_f32_16x16x32_bf16 v[12:15], v[172:175], v[204:207], v[12:15]
	v_exp_f32_e32 v75, v75
	v_mfma_f32_16x16x32_bf16 v[8:11], v[172:175], v[242:245], v[8:11]
	v_exp_f32_e32 v79, v79
	ds_read_b128 v[172:175], v210 offset:26624
	s_waitcnt lgkmcnt(6)
	v_mfma_f32_16x16x32_bf16 v[80:83], v[176:179], v[104:107], v[80:83]
	v_add_f32_e32 v220, v220, v72
	v_add_f32_e32 v221, v221, v76
	v_mfma_f32_16x16x32_bf16 v[84:87], v[176:179], v[120:123], v[84:87]
	v_add_f32_e32 v220, v220, v73
	ds_read_b128 v[176:179], v203 offset:45056
	v_mfma_f32_16x16x32_bf16 v[16:19], v[180:183], v[242:245], v[16:19]
	v_add_f32_e32 v221, v221, v77
	v_add_f32_e32 v220, v220, v74
	v_mfma_f32_16x16x32_bf16 v[20:23], v[180:183], v[204:207], v[20:23]
	v_add_f32_e32 v221, v221, v78
	ds_read_b128 v[180:183], v210 offset:28672
	s_waitcnt lgkmcnt(6)
	v_mfma_f32_16x16x32_bf16 v[84:87], v[230:233], v[124:127], v[84:87]
	v_add_f32_e32 v220, v220, v75
	v_add_f32_e32 v221, v221, v79
	v_mfma_f32_16x16x32_bf16 v[80:83], v[230:233], v[108:111], v[80:83]
	v_cvt_pk_bf16_f32 v216, v64, v65
	ds_read_b128 v[230:233], v246 offset:45056
	v_mfma_f32_16x16x32_bf16 v[28:31], v[234:237], v[204:207], v[28:31]
	v_cvt_pk_bf16_f32 v217, v66, v67
	v_cvt_pk_bf16_f32 v238, v68, v69
	v_mfma_f32_16x16x32_bf16 v[24:27], v[234:237], v[242:245], v[24:27]
	v_cvt_pk_bf16_f32 v239, v70, v71
	ds_read_b128 v[234:237], v210 offset:30720
	s_waitcnt lgkmcnt(6)
	v_mfma_f32_16x16x32_bf16 v[88:91], v[160:163], v[96:99], 0
	v_exp_f32_e32 v80, v80
	v_mfma_f32_16x16x32_bf16 v[92:95], v[160:163], v[112:115], 0
	v_exp_f32_e32 v84, v84
	v_mfma_f32_16x16x32_bf16 v[32:35], v[164:167], v[242:245], v[32:35]
	v_exp_f32_e32 v81, v81
	v_mfma_f32_16x16x32_bf16 v[36:39], v[164:167], v[204:207], v[36:39]
	v_exp_f32_e32 v85, v85
	s_waitcnt lgkmcnt(4)
	v_mfma_f32_16x16x32_bf16 v[92:95], v[168:171], v[116:119], v[92:95]
	v_exp_f32_e32 v82, v82
	v_mfma_f32_16x16x32_bf16 v[88:91], v[168:171], v[100:103], v[88:91]
	v_exp_f32_e32 v86, v86
	v_mfma_f32_16x16x32_bf16 v[44:47], v[172:175], v[204:207], v[44:47]
	v_exp_f32_e32 v83, v83
	v_mfma_f32_16x16x32_bf16 v[40:43], v[172:175], v[242:245], v[40:43]
	v_exp_f32_e32 v87, v87
	s_waitcnt lgkmcnt(3)
	v_mfma_f32_16x16x32_bf16 v[88:91], v[176:179], v[104:107], v[88:91]
	v_add_f32_e32 v220, v220, v80
	v_add_f32_e32 v221, v221, v84
	v_mfma_f32_16x16x32_bf16 v[92:95], v[176:179], v[120:123], v[92:95]
	v_add_f32_e32 v220, v220, v81
	s_waitcnt lgkmcnt(0)
	s_barrier
	ds_read_b128 v[160:163], v201 offset:49152
	ds_read_b128 v[164:167], v209 offset:32768
	ds_read_b128 v[168:171], v202 offset:49152
	ds_read_b128 v[172:175], v209 offset:34816
	ds_read_b128 v[176:179], v203 offset:49152
	v_mfma_f32_16x16x32_bf16 v[48:51], v[180:183], v[242:245], v[48:51]
	v_add_f32_e32 v221, v221, v85
	v_add_f32_e32 v220, v220, v82
	v_mfma_f32_16x16x32_bf16 v[52:55], v[180:183], v[204:207], v[52:55]
	v_add_f32_e32 v221, v221, v86
	ds_read_b128 v[180:183], v209 offset:36864
	v_mfma_f32_16x16x32_bf16 v[92:95], v[230:233], v[124:127], v[92:95]
	v_add_f32_e32 v220, v220, v83
	v_add_f32_e32 v221, v221, v87
	v_mfma_f32_16x16x32_bf16 v[88:91], v[230:233], v[108:111], v[88:91]
	v_cvt_pk_bf16_f32 v218, v72, v73
	ds_read_b128 v[230:233], v246 offset:49152
	v_mfma_f32_16x16x32_bf16 v[60:63], v[234:237], v[204:207], v[60:63]
	v_cvt_pk_bf16_f32 v219, v74, v75
	v_cvt_pk_bf16_f32 v240, v76, v77
	v_mfma_f32_16x16x32_bf16 v[56:59], v[234:237], v[242:245], v[56:59]
	v_cvt_pk_bf16_f32 v241, v78, v79
	ds_read_b128 v[234:237], v209 offset:38912
	s_cmp_eq_u32 s100, 0
	s_cbranch_scc1 .Lattn_pl64
	s_setprio 1
.Lattn_pl64:
	s_waitcnt lgkmcnt(6)
	v_mfma_f32_16x16x32_bf16 v[64:67], v[160:163], v[96:99], 0
	v_exp_f32_e32 v88, v88
	v_mfma_f32_16x16x32_bf16 v[68:71], v[160:163], v[112:115], 0
	v_exp_f32_e32 v92, v92
	ds_read_b128 v[160:163], v201 offset:53248
	s_add_u32 s8, s16, 0x3bc00300
	s_addc_u32 s9, s17, 0
	s_add_u32 s6, s15, 0x23a70000
	s_addc_u32 s7, s14, 0
	v_mfma_f32_16x16x32_bf16 v[0:3], v[164:167], v[216:219], v[0:3]
	v_cvt_pk_bf16_f32 v242, v80, v81
	v_mfma_f32_16x16x32_bf16 v[4:7], v[164:167], v[238:241], v[4:7]
	v_exp_f32_e32 v89, v89
	ds_read_b128 v[164:167], v209 offset:40960
	s_waitcnt vmcnt(4)
	ds_write_b128 v225, v[152:155] offset:16384
	s_waitcnt lgkmcnt(7)
	v_mfma_f32_16x16x32_bf16 v[68:71], v[168:171], v[116:119], v[68:71]
	v_exp_f32_e32 v93, v93
	v_mfma_f32_16x16x32_bf16 v[64:67], v[168:171], v[100:103], v[64:67]
	v_cvt_pk_bf16_f32 v243, v82, v83
	ds_read_b128 v[168:171], v202 offset:53248
	ds_write_b128 v226, v[156:159] offset:16384
	v_mfma_f32_16x16x32_bf16 v[12:15], v[172:175], v[238:241], v[12:15]
	v_exp_f32_e32 v90, v90
	v_mfma_f32_16x16x32_bf16 v[8:11], v[172:175], v[216:219], v[8:11]
	v_exp_f32_e32 v94, v94
	ds_read_b128 v[172:175], v209 offset:43008
	ds_write_b64 v227, v[132:133] offset:0
	s_waitcnt lgkmcnt(9)
	v_mfma_f32_16x16x32_bf16 v[64:67], v[176:179], v[104:107], v[64:67]
	v_cvt_pk_bf16_f32 v204, v84, v85
	v_mfma_f32_16x16x32_bf16 v[68:71], v[176:179], v[120:123], v[68:71]
	v_exp_f32_e32 v91, v91
	ds_read_b128 v[176:179], v203 offset:53248
	ds_write_b64 v228, v[134:135] offset:0
	v_mfma_f32_16x16x32_bf16 v[16:19], v[180:183], v[216:219], v[16:19]
	v_exp_f32_e32 v95, v95
	v_mfma_f32_16x16x32_bf16 v[20:23], v[180:183], v[238:241], v[20:23]
	v_cvt_pk_bf16_f32 v205, v86, v87
	v_add_f32_e32 v220, v220, v88
	ds_read_b128 v[180:183], v209 offset:45056
	ds_write_b64 v229, v[128:129] offset:0
	s_waitcnt lgkmcnt(11)
	v_mfma_f32_16x16x32_bf16 v[68:71], v[230:233], v[124:127], v[68:71]
	v_add_f32_e32 v221, v221, v92
	v_add_f32_e32 v220, v220, v89
	v_mfma_f32_16x16x32_bf16 v[64:67], v[230:233], v[108:111], v[64:67]
	v_add_f32_e32 v221, v221, v93
	v_cvt_pk_bf16_f32 v244, v88, v89
	ds_read_b128 v[230:233], v246 offset:53248
	ds_write_b64 v184, v[130:131] offset:0
	v_mfma_f32_16x16x32_bf16 v[28:31], v[234:237], v[238:241], v[28:31]
	v_cvt_pk_bf16_f32 v245, v90, v91
	v_cvt_pk_bf16_f32 v206, v92, v93
	v_mfma_f32_16x16x32_bf16 v[24:27], v[234:237], v[216:219], v[24:27]
	v_cvt_pk_bf16_f32 v207, v94, v95
	ds_read_b128 v[234:237], v209 offset:47104
	global_load_dwordx4 v[132:135], v198, s[8:9]
	s_waitcnt lgkmcnt(12)
	v_mfma_f32_16x16x32_bf16 v[72:75], v[160:163], v[96:99], 0
	v_add_f32_e32 v220, v220, v90
	v_add_f32_e32 v221, v221, v94
	v_mfma_f32_16x16x32_bf16 v[76:79], v[160:163], v[112:115], 0
	v_add_f32_e32 v220, v220, v91
	v_add_f32_e32 v221, v221, v95
	ds_read_b128 v[160:163], v201 offset:57344
	global_load_dwordx4 v[128:131], v199, s[8:9]
	v_mfma_f32_16x16x32_bf16 v[32:35], v[164:167], v[216:219], v[32:35]
	v_add_f32_e32 v194, v194, v220
	v_add_f32_e32 v195, v195, v221
	v_mfma_f32_16x16x32_bf16 v[36:39], v[164:167], v[238:241], v[36:39]
	v_exp_f32_e32 v64, v64
	ds_read_b128 v[164:167], v210 offset:32768
	global_load_dwordx4 v[152:155], v196, s[6:7]
	s_waitcnt lgkmcnt(10)
	v_mfma_f32_16x16x32_bf16 v[76:79], v[168:171], v[116:119], v[76:79]
	v_exp_f32_e32 v68, v68
	v_mfma_f32_16x16x32_bf16 v[72:75], v[168:171], v[100:103], v[72:75]
	v_exp_f32_e32 v65, v65
	ds_read_b128 v[168:171], v202 offset:57344
	global_load_dwordx4 v[156:159], v197, s[6:7]
	v_mfma_f32_16x16x32_bf16 v[44:47], v[172:175], v[238:241], v[44:47]
	v_exp_f32_e32 v69, v69
	v_mfma_f32_16x16x32_bf16 v[40:43], v[172:175], v[216:219], v[40:43]
	v_exp_f32_e32 v66, v66
	ds_read_b128 v[172:175], v210 offset:34816
	s_waitcnt lgkmcnt(8)
	v_mfma_f32_16x16x32_bf16 v[72:75], v[176:179], v[104:107], v[72:75]
	v_exp_f32_e32 v70, v70
	v_mfma_f32_16x16x32_bf16 v[76:79], v[176:179], v[120:123], v[76:79]
	v_exp_f32_e32 v67, v67
	ds_read_b128 v[176:179], v203 offset:57344
	v_mfma_f32_16x16x32_bf16 v[48:51], v[180:183], v[216:219], v[48:51]
	v_exp_f32_e32 v71, v71
	v_mfma_f32_16x16x32_bf16 v[52:55], v[180:183], v[238:241], v[52:55]
	v_add_f32_e32 v220, v64, v65
	ds_read_b128 v[180:183], v210 offset:36864
	s_waitcnt lgkmcnt(6)
	v_mfma_f32_16x16x32_bf16 v[76:79], v[230:233], v[124:127], v[76:79]
	v_add_f32_e32 v221, v68, v69
	v_mfma_f32_16x16x32_bf16 v[72:75], v[230:233], v[108:111], v[72:75]
	v_add_f32_e32 v220, v220, v66
	ds_read_b128 v[230:233], v246 offset:57344
	v_mfma_f32_16x16x32_bf16 v[60:63], v[234:237], v[238:241], v[60:63]
	v_add_f32_e32 v221, v221, v70
	v_add_f32_e32 v220, v220, v67
	v_mfma_f32_16x16x32_bf16 v[56:59], v[234:237], v[216:219], v[56:59]
	v_add_f32_e32 v221, v221, v71
	ds_read_b128 v[234:237], v210 offset:38912
	s_waitcnt lgkmcnt(6)
	v_mfma_f32_16x16x32_bf16 v[80:83], v[160:163], v[96:99], 0
	v_exp_f32_e32 v72, v72
	v_mfma_f32_16x16x32_bf16 v[84:87], v[160:163], v[112:115], 0
	v_exp_f32_e32 v76, v76
	ds_read_b128 v[160:163], v201 offset:61440
	v_mfma_f32_16x16x32_bf16 v[0:3], v[164:167], v[242:245], v[0:3]
	v_exp_f32_e32 v73, v73
	v_mfma_f32_16x16x32_bf16 v[4:7], v[164:167], v[204:207], v[4:7]
	v_exp_f32_e32 v77, v77
	ds_read_b128 v[164:167], v210 offset:40960
	s_waitcnt lgkmcnt(6)
	v_mfma_f32_16x16x32_bf16 v[84:87], v[168:171], v[116:119], v[84:87]
	v_exp_f32_e32 v74, v74
	v_mfma_f32_16x16x32_bf16 v[80:83], v[168:171], v[100:103], v[80:83]
	v_exp_f32_e32 v78, v78
	ds_read_b128 v[168:171], v202 offset:61440
	v_mfma_f32_16x16x32_bf16 v[12:15], v[172:175], v[204:207], v[12:15]
	v_exp_f32_e32 v75, v75
	v_mfma_f32_16x16x32_bf16 v[8:11], v[172:175], v[242:245], v[8:11]
	v_exp_f32_e32 v79, v79
	ds_read_b128 v[172:175], v210 offset:43008
	s_waitcnt lgkmcnt(6)
	v_mfma_f32_16x16x32_bf16 v[80:83], v[176:179], v[104:107], v[80:83]
	v_add_f32_e32 v220, v220, v72
	v_add_f32_e32 v221, v221, v76
	v_mfma_f32_16x16x32_bf16 v[84:87], v[176:179], v[120:123], v[84:87]
	v_add_f32_e32 v220, v220, v73
	ds_read_b128 v[176:179], v203 offset:61440
	v_mfma_f32_16x16x32_bf16 v[16:19], v[180:183], v[242:245], v[16:19]
	v_add_f32_e32 v221, v221, v77
	v_add_f32_e32 v220, v220, v74
	v_mfma_f32_16x16x32_bf16 v[20:23], v[180:183], v[204:207], v[20:23]
	v_add_f32_e32 v221, v221, v78
	ds_read_b128 v[180:183], v210 offset:45056
	s_waitcnt lgkmcnt(6)
	v_mfma_f32_16x16x32_bf16 v[84:87], v[230:233], v[124:127], v[84:87]
	v_add_f32_e32 v220, v220, v75
	v_add_f32_e32 v221, v221, v79
	v_mfma_f32_16x16x32_bf16 v[80:83], v[230:233], v[108:111], v[80:83]
	v_cvt_pk_bf16_f32 v216, v64, v65
	ds_read_b128 v[230:233], v246 offset:61440
	v_mfma_f32_16x16x32_bf16 v[28:31], v[234:237], v[204:207], v[28:31]
	v_cvt_pk_bf16_f32 v217, v66, v67
	v_cvt_pk_bf16_f32 v238, v68, v69
	v_mfma_f32_16x16x32_bf16 v[24:27], v[234:237], v[242:245], v[24:27]
	v_cvt_pk_bf16_f32 v239, v70, v71
	ds_read_b128 v[234:237], v210 offset:47104
	s_waitcnt lgkmcnt(6)
	v_mfma_f32_16x16x32_bf16 v[88:91], v[160:163], v[96:99], 0
	v_exp_f32_e32 v80, v80
	v_mfma_f32_16x16x32_bf16 v[92:95], v[160:163], v[112:115], 0
	v_exp_f32_e32 v84, v84
	ds_read_b128 v[160:163], v201 offset:0
	v_mfma_f32_16x16x32_bf16 v[32:35], v[164:167], v[242:245], v[32:35]
	v_exp_f32_e32 v81, v81
	v_mfma_f32_16x16x32_bf16 v[36:39], v[164:167], v[204:207], v[36:39]
	v_exp_f32_e32 v85, v85
	ds_read_b128 v[164:167], v209 offset:49152
	s_waitcnt lgkmcnt(6)
	v_mfma_f32_16x16x32_bf16 v[92:95], v[168:171], v[116:119], v[92:95]
	v_exp_f32_e32 v82, v82
	v_mfma_f32_16x16x32_bf16 v[88:91], v[168:171], v[100:103], v[88:91]
	v_exp_f32_e32 v86, v86
	ds_read_b128 v[168:171], v202 offset:0
	v_mfma_f32_16x16x32_bf16 v[44:47], v[172:175], v[204:207], v[44:47]
	v_exp_f32_e32 v83, v83
	v_mfma_f32_16x16x32_bf16 v[40:43], v[172:175], v[242:245], v[40:43]
	v_exp_f32_e32 v87, v87
	ds_read_b128 v[172:175], v209 offset:51200
	s_waitcnt lgkmcnt(6)
	v_mfma_f32_16x16x32_bf16 v[88:91], v[176:179], v[104:107], v[88:91]
	v_add_f32_e32 v220, v220, v80
	v_add_f32_e32 v221, v221, v84
	v_mfma_f32_16x16x32_bf16 v[92:95], v[176:179], v[120:123], v[92:95]
	v_add_f32_e32 v220, v220, v81
	ds_read_b128 v[176:179], v203 offset:0
	v_mfma_f32_16x16x32_bf16 v[48:51], v[180:183], v[242:245], v[48:51]
	v_add_f32_e32 v221, v221, v85
	v_add_f32_e32 v220, v220, v82
	v_mfma_f32_16x16x32_bf16 v[52:55], v[180:183], v[204:207], v[52:55]
	v_add_f32_e32 v221, v221, v86
	ds_read_b128 v[180:183], v209 offset:53248
	s_waitcnt lgkmcnt(6)
	v_mfma_f32_16x16x32_bf16 v[92:95], v[230:233], v[124:127], v[92:95]
	v_add_f32_e32 v220, v220, v83
	v_add_f32_e32 v221, v221, v87
	v_mfma_f32_16x16x32_bf16 v[88:91], v[230:233], v[108:111], v[88:91]
	v_cvt_pk_bf16_f32 v218, v72, v73
	ds_read_b128 v[230:233], v246 offset:0
	v_mfma_f32_16x16x32_bf16 v[60:63], v[234:237], v[204:207], v[60:63]
	v_cvt_pk_bf16_f32 v219, v74, v75
	v_cvt_pk_bf16_f32 v240, v76, v77
	v_mfma_f32_16x16x32_bf16 v[56:59], v[234:237], v[242:245], v[56:59]
	v_cvt_pk_bf16_f32 v241, v78, v79
	ds_read_b128 v[234:237], v209 offset:55296
	s_waitcnt lgkmcnt(6)
	v_mfma_f32_16x16x32_bf16 v[64:67], v[160:163], v[96:99], 0
	v_exp_f32_e32 v88, v88
	v_mfma_f32_16x16x32_bf16 v[68:71], v[160:163], v[112:115], 0
	v_exp_f32_e32 v92, v92
	ds_read_b128 v[160:163], v201 offset:4096
	s_add_u32 s8, s16, 0x3bc00380
	s_addc_u32 s9, s17, 0
	s_add_u32 s6, s15, 0x23a80000
	s_addc_u32 s7, s14, 0
	v_mfma_f32_16x16x32_bf16 v[0:3], v[164:167], v[216:219], v[0:3]
	v_cvt_pk_bf16_f32 v242, v80, v81
	v_mfma_f32_16x16x32_bf16 v[4:7], v[164:167], v[238:241], v[4:7]
	v_exp_f32_e32 v89, v89
	ds_read_b128 v[164:167], v209 offset:57344
	s_waitcnt vmcnt(4)
	ds_write_b128 v225, v[136:139] offset:32768
	s_waitcnt lgkmcnt(7)
	v_mfma_f32_16x16x32_bf16 v[68:71], v[168:171], v[116:119], v[68:71]
	v_exp_f32_e32 v93, v93
	v_mfma_f32_16x16x32_bf16 v[64:67], v[168:171], v[100:103], v[64:67]
	v_cvt_pk_bf16_f32 v243, v82, v83
	ds_read_b128 v[168:171], v202 offset:4096
	ds_write_b128 v226, v[140:143] offset:32768
	v_mfma_f32_16x16x32_bf16 v[12:15], v[172:175], v[238:241], v[12:15]
	v_exp_f32_e32 v90, v90
	v_mfma_f32_16x16x32_bf16 v[8:11], v[172:175], v[216:219], v[8:11]
	v_exp_f32_e32 v94, v94
	ds_read_b128 v[172:175], v209 offset:59392
	ds_write_b64 v227, v[148:149] offset:16384
	s_waitcnt lgkmcnt(9)
	v_mfma_f32_16x16x32_bf16 v[64:67], v[176:179], v[104:107], v[64:67]
	v_cvt_pk_bf16_f32 v204, v84, v85
	v_mfma_f32_16x16x32_bf16 v[68:71], v[176:179], v[120:123], v[68:71]
	v_exp_f32_e32 v91, v91
	ds_read_b128 v[176:179], v203 offset:4096
	ds_write_b64 v228, v[150:151] offset:16384
	v_mfma_f32_16x16x32_bf16 v[16:19], v[180:183], v[216:219], v[16:19]
	v_exp_f32_e32 v95, v95
	v_mfma_f32_16x16x32_bf16 v[20:23], v[180:183], v[238:241], v[20:23]
	v_cvt_pk_bf16_f32 v205, v86, v87
	v_add_f32_e32 v220, v220, v88
	ds_read_b128 v[180:183], v209 offset:61440
	ds_write_b64 v229, v[144:145] offset:16384
	s_waitcnt lgkmcnt(11)
	v_mfma_f32_16x16x32_bf16 v[68:71], v[230:233], v[124:127], v[68:71]
	v_add_f32_e32 v221, v221, v92
	v_add_f32_e32 v220, v220, v89
	v_mfma_f32_16x16x32_bf16 v[64:67], v[230:233], v[108:111], v[64:67]
	v_add_f32_e32 v221, v221, v93
	v_cvt_pk_bf16_f32 v244, v88, v89
	ds_read_b128 v[230:233], v246 offset:4096
	ds_write_b64 v184, v[146:147] offset:16384
	v_mfma_f32_16x16x32_bf16 v[28:31], v[234:237], v[238:241], v[28:31]
	v_cvt_pk_bf16_f32 v245, v90, v91
	v_cvt_pk_bf16_f32 v206, v92, v93
	v_mfma_f32_16x16x32_bf16 v[24:27], v[234:237], v[216:219], v[24:27]
	v_cvt_pk_bf16_f32 v207, v94, v95
	ds_read_b128 v[234:237], v209 offset:63488
	global_load_dwordx4 v[148:151], v198, s[8:9]
	s_waitcnt lgkmcnt(12)
	v_mfma_f32_16x16x32_bf16 v[72:75], v[160:163], v[96:99], 0
	v_add_f32_e32 v220, v220, v90
	v_add_f32_e32 v221, v221, v94
	v_mfma_f32_16x16x32_bf16 v[76:79], v[160:163], v[112:115], 0
	v_add_f32_e32 v220, v220, v91
	v_add_f32_e32 v221, v221, v95
	ds_read_b128 v[160:163], v201 offset:8192
	global_load_dwordx4 v[144:147], v199, s[8:9]
	v_mfma_f32_16x16x32_bf16 v[32:35], v[164:167], v[216:219], v[32:35]
	v_add_f32_e32 v194, v194, v220
	v_add_f32_e32 v195, v195, v221
	v_mfma_f32_16x16x32_bf16 v[36:39], v[164:167], v[238:241], v[36:39]
	v_exp_f32_e32 v64, v64
	ds_read_b128 v[164:167], v210 offset:49152
	global_load_dwordx4 v[136:139], v196, s[6:7]
	s_waitcnt lgkmcnt(10)
	v_mfma_f32_16x16x32_bf16 v[76:79], v[168:171], v[116:119], v[76:79]
	v_exp_f32_e32 v68, v68
	v_mfma_f32_16x16x32_bf16 v[72:75], v[168:171], v[100:103], v[72:75]
	v_exp_f32_e32 v65, v65
	ds_read_b128 v[168:171], v202 offset:8192
	global_load_dwordx4 v[140:143], v197, s[6:7]
	v_mfma_f32_16x16x32_bf16 v[44:47], v[172:175], v[238:241], v[44:47]
	v_exp_f32_e32 v69, v69
	v_mfma_f32_16x16x32_bf16 v[40:43], v[172:175], v[216:219], v[40:43]
	v_exp_f32_e32 v66, v66
	ds_read_b128 v[172:175], v210 offset:51200
	s_setprio 0
	s_waitcnt lgkmcnt(8)
	v_mfma_f32_16x16x32_bf16 v[72:75], v[176:179], v[104:107], v[72:75]
	v_exp_f32_e32 v70, v70
	v_mfma_f32_16x16x32_bf16 v[76:79], v[176:179], v[120:123], v[76:79]
	v_exp_f32_e32 v67, v67
	ds_read_b128 v[176:179], v203 offset:8192
	v_mfma_f32_16x16x32_bf16 v[48:51], v[180:183], v[216:219], v[48:51]
	v_exp_f32_e32 v71, v71
	v_mfma_f32_16x16x32_bf16 v[52:55], v[180:183], v[238:241], v[52:55]
	v_add_f32_e32 v220, v64, v65
	ds_read_b128 v[180:183], v210 offset:53248
	s_waitcnt lgkmcnt(6)
	v_mfma_f32_16x16x32_bf16 v[76:79], v[230:233], v[124:127], v[76:79]
	v_add_f32_e32 v221, v68, v69
	v_mfma_f32_16x16x32_bf16 v[72:75], v[230:233], v[108:111], v[72:75]
	v_add_f32_e32 v220, v220, v66
	ds_read_b128 v[230:233], v246 offset:8192
	v_mfma_f32_16x16x32_bf16 v[60:63], v[234:237], v[238:241], v[60:63]
	v_add_f32_e32 v221, v221, v70
	v_add_f32_e32 v220, v220, v67
	v_mfma_f32_16x16x32_bf16 v[56:59], v[234:237], v[216:219], v[56:59]
	v_add_f32_e32 v221, v221, v71
	ds_read_b128 v[234:237], v210 offset:55296
	s_waitcnt lgkmcnt(6)
	v_mfma_f32_16x16x32_bf16 v[80:83], v[160:163], v[96:99], 0
	v_exp_f32_e32 v72, v72
	v_mfma_f32_16x16x32_bf16 v[84:87], v[160:163], v[112:115], 0
	v_exp_f32_e32 v76, v76
	ds_read_b128 v[160:163], v201 offset:12288
	v_mfma_f32_16x16x32_bf16 v[0:3], v[164:167], v[242:245], v[0:3]
	v_exp_f32_e32 v73, v73
	v_mfma_f32_16x16x32_bf16 v[4:7], v[164:167], v[204:207], v[4:7]
	v_exp_f32_e32 v77, v77
	ds_read_b128 v[164:167], v210 offset:57344
	s_waitcnt lgkmcnt(6)
	v_mfma_f32_16x16x32_bf16 v[84:87], v[168:171], v[116:119], v[84:87]
	v_exp_f32_e32 v74, v74
	v_mfma_f32_16x16x32_bf16 v[80:83], v[168:171], v[100:103], v[80:83]
	v_exp_f32_e32 v78, v78
	ds_read_b128 v[168:171], v202 offset:12288
	v_mfma_f32_16x16x32_bf16 v[12:15], v[172:175], v[204:207], v[12:15]
	v_exp_f32_e32 v75, v75
	v_mfma_f32_16x16x32_bf16 v[8:11], v[172:175], v[242:245], v[8:11]
	v_exp_f32_e32 v79, v79
	ds_read_b128 v[172:175], v210 offset:59392
	s_waitcnt lgkmcnt(6)
	v_mfma_f32_16x16x32_bf16 v[80:83], v[176:179], v[104:107], v[80:83]
	v_add_f32_e32 v220, v220, v72
	v_add_f32_e32 v221, v221, v76
	v_mfma_f32_16x16x32_bf16 v[84:87], v[176:179], v[120:123], v[84:87]
	v_add_f32_e32 v220, v220, v73
	ds_read_b128 v[176:179], v203 offset:12288
	s_add_u32 s10, s10, 0x200
	s_addc_u32 s11, s11, 0
	s_add_u32 s12, s12, 0x40000
	s_addc_u32 s13, s13, 0
	s_add_i32 s4, s4, 4
	s_cmpk_lt_u32 s4, 0x104
	s_cselect_b64 s[6:7], -1, 0
	s_and_b64 s[6:7], s[0:1], s[6:7]
	s_and_b64 vcc, exec, s[6:7]
	v_mfma_f32_16x16x32_bf16 v[16:19], v[180:183], v[242:245], v[16:19]
	v_add_f32_e32 v221, v221, v77
	v_add_f32_e32 v220, v220, v74
	v_mfma_f32_16x16x32_bf16 v[20:23], v[180:183], v[204:207], v[20:23]
	v_add_f32_e32 v221, v221, v78
	ds_read_b128 v[180:183], v210 offset:61440
	s_waitcnt lgkmcnt(6)
	v_mfma_f32_16x16x32_bf16 v[84:87], v[230:233], v[124:127], v[84:87]
	v_add_f32_e32 v220, v220, v75
	v_add_f32_e32 v221, v221, v79
	v_mfma_f32_16x16x32_bf16 v[80:83], v[230:233], v[108:111], v[80:83]
	v_cvt_pk_bf16_f32 v216, v64, v65
	ds_read_b128 v[230:233], v246 offset:12288
	v_mfma_f32_16x16x32_bf16 v[28:31], v[234:237], v[204:207], v[28:31]
	v_cvt_pk_bf16_f32 v217, v66, v67
	v_cvt_pk_bf16_f32 v238, v68, v69
	v_mfma_f32_16x16x32_bf16 v[24:27], v[234:237], v[242:245], v[24:27]
	v_cvt_pk_bf16_f32 v239, v70, v71
	ds_read_b128 v[234:237], v210 offset:63488
	s_waitcnt lgkmcnt(6)
	v_mfma_f32_16x16x32_bf16 v[88:91], v[160:163], v[96:99], 0
	v_exp_f32_e32 v80, v80
	v_mfma_f32_16x16x32_bf16 v[92:95], v[160:163], v[112:115], 0
	v_exp_f32_e32 v84, v84
	v_mfma_f32_16x16x32_bf16 v[32:35], v[164:167], v[242:245], v[32:35]
	v_exp_f32_e32 v81, v81
	v_mfma_f32_16x16x32_bf16 v[36:39], v[164:167], v[204:207], v[36:39]
	v_exp_f32_e32 v85, v85
	s_waitcnt lgkmcnt(4)
	v_mfma_f32_16x16x32_bf16 v[92:95], v[168:171], v[116:119], v[92:95]
	v_exp_f32_e32 v82, v82
	v_mfma_f32_16x16x32_bf16 v[88:91], v[168:171], v[100:103], v[88:91]
	v_exp_f32_e32 v86, v86
	v_mfma_f32_16x16x32_bf16 v[44:47], v[172:175], v[204:207], v[44:47]
	v_exp_f32_e32 v83, v83
	v_mfma_f32_16x16x32_bf16 v[40:43], v[172:175], v[242:245], v[40:43]
	v_exp_f32_e32 v87, v87
	s_waitcnt lgkmcnt(3)
	v_mfma_f32_16x16x32_bf16 v[88:91], v[176:179], v[104:107], v[88:91]
	v_add_f32_e32 v220, v220, v80
	v_add_f32_e32 v221, v221, v84
	v_mfma_f32_16x16x32_bf16 v[92:95], v[176:179], v[120:123], v[92:95]
	v_add_f32_e32 v220, v220, v81
	s_waitcnt lgkmcnt(0)
	s_barrier
	ds_read_b128 v[160:163], v201 offset:16384
	ds_read_b128 v[164:167], v209 offset:0
	ds_read_b128 v[168:171], v202 offset:16384
	ds_read_b128 v[172:175], v209 offset:2048
	ds_read_b128 v[176:179], v203 offset:16384
	v_mfma_f32_16x16x32_bf16 v[48:51], v[180:183], v[242:245], v[48:51]
	v_add_f32_e32 v221, v221, v85
	v_add_f32_e32 v220, v220, v82
	v_mfma_f32_16x16x32_bf16 v[52:55], v[180:183], v[204:207], v[52:55]
	v_add_f32_e32 v221, v221, v86
	ds_read_b128 v[180:183], v209 offset:4096
	v_mfma_f32_16x16x32_bf16 v[92:95], v[230:233], v[124:127], v[92:95]
	v_add_f32_e32 v220, v220, v83
	v_add_f32_e32 v221, v221, v87
	v_mfma_f32_16x16x32_bf16 v[88:91], v[230:233], v[108:111], v[88:91]
	v_cvt_pk_bf16_f32 v218, v72, v73
	ds_read_b128 v[230:233], v246 offset:16384
	v_mfma_f32_16x16x32_bf16 v[60:63], v[234:237], v[204:207], v[60:63]
	v_cvt_pk_bf16_f32 v219, v74, v75
	v_cvt_pk_bf16_f32 v240, v76, v77
	v_mfma_f32_16x16x32_bf16 v[56:59], v[234:237], v[242:245], v[56:59]
	v_cvt_pk_bf16_f32 v241, v78, v79
	ds_read_b128 v[234:237], v209 offset:6144
	s_cbranch_vccnz .LBB0_734
	s_setprio 0
	s_waitcnt vmcnt(0)
	s_nop 7
	s_nop 7
	ds_swizzle_b32 v64, v194 offset:swizzle(SWAP,16)
	s_waitcnt lgkmcnt(0)
	v_add_f32_e32 v194, v194, v64
	v_mov_b32_e32 v65, v194
	s_nop 1
	v_permlane32_swap_b32_e32 v194, v65
	v_add_f32_e32 v194, v194, v65
	s_nop 0
	v_rcp_f32_e32 v66, v194
	ds_swizzle_b32 v64, v195 offset:swizzle(SWAP,16)
	s_waitcnt lgkmcnt(0)
	v_add_f32_e32 v195, v195, v64
	v_mov_b32_e32 v65, v195
	s_nop 1
	v_permlane32_swap_b32_e32 v195, v65
	v_add_f32_e32 v195, v195, v65
	s_nop 0
	v_rcp_f32_e32 v67, v195
	v_readlane_b32 s100, v250, 8
	v_mbcnt_lo_u32_b32 v68, -1, 0
	v_mbcnt_hi_u32_b32 v68, -1, v68
	v_and_b32_e32 v69, 15, v68
	v_lshrrev_b32_e32 v70, 4, v68
	s_lshr_b32 s101, s100, 1
	v_add_u32_e32 v69, s101, v69
	v_lshlrev_b32_e32 v69, 12, v69
	v_and_b32_e32 v71, 1, v70
	v_lshlrev_b32_e32 v71, 5, v71
	v_and_b32_e32 v70, 2, v70
	v_lshl_add_u32 v71, v70, 3, v71
	v_add_u32_e32 v70, v69, v71
	v_add_u32_e32 v71, 0x10000, v70
	v_mul_f32_e32 v0, v0, v66
	v_mul_f32_e32 v1, v1, v66
	v_mul_f32_e32 v2, v2, v66
	v_mul_f32_e32 v3, v3, v66
	v_mul_f32_e32 v8, v8, v66
	v_mul_f32_e32 v9, v9, v66
	v_mul_f32_e32 v10, v10, v66
	v_mul_f32_e32 v11, v11, v66
	v_cvt_pk_bf16_f32 v72, v0, v1
	v_cvt_pk_bf16_f32 v73, v2, v3
	v_cvt_pk_bf16_f32 v74, v8, v9
	v_cvt_pk_bf16_f32 v75, v10, v11
	s_nop 1
	v_permlane16_swap_b32_e32 v72, v74
	v_permlane16_swap_b32_e32 v73, v75
	s_nop 1
	global_store_dwordx4 v70, v[72:75], s[58:59] offset:0
	v_mul_f32_e32 v16, v16, v66
	v_mul_f32_e32 v17, v17, v66
	v_mul_f32_e32 v18, v18, v66
	v_mul_f32_e32 v19, v19, v66
	v_mul_f32_e32 v24, v24, v66
	v_mul_f32_e32 v25, v25, v66
	v_mul_f32_e32 v26, v26, v66
	v_mul_f32_e32 v27, v27, v66
	v_cvt_pk_bf16_f32 v76, v16, v17
	v_cvt_pk_bf16_f32 v77, v18, v19
	v_cvt_pk_bf16_f32 v78, v24, v25
	v_cvt_pk_bf16_f32 v79, v26, v27
	s_nop 1
	v_permlane16_swap_b32_e32 v76, v78
	v_permlane16_swap_b32_e32 v77, v79
	s_nop 1
	global_store_dwordx4 v70, v[76:79], s[58:59] offset:64
	v_mul_f32_e32 v32, v32, v66
	v_mul_f32_e32 v33, v33, v66
	v_mul_f32_e32 v34, v34, v66
	v_mul_f32_e32 v35, v35, v66
	v_mul_f32_e32 v40, v40, v66
	v_mul_f32_e32 v41, v41, v66
	v_mul_f32_e32 v42, v42, v66
	v_mul_f32_e32 v43, v43, v66
	v_cvt_pk_bf16_f32 v80, v32, v33
	v_cvt_pk_bf16_f32 v81, v34, v35
	v_cvt_pk_bf16_f32 v82, v40, v41
	v_cvt_pk_bf16_f32 v83, v42, v43
	s_nop 1
	v_permlane16_swap_b32_e32 v80, v82
	v_permlane16_swap_b32_e32 v81, v83
	s_nop 1
	global_store_dwordx4 v70, v[80:83], s[58:59] offset:128
	v_mul_f32_e32 v48, v48, v66
	v_mul_f32_e32 v49, v49, v66
	v_mul_f32_e32 v50, v50, v66
	v_mul_f32_e32 v51, v51, v66
	v_mul_f32_e32 v56, v56, v66
	v_mul_f32_e32 v57, v57, v66
	v_mul_f32_e32 v58, v58, v66
	v_mul_f32_e32 v59, v59, v66
	v_cvt_pk_bf16_f32 v84, v48, v49
	v_cvt_pk_bf16_f32 v85, v50, v51
	v_cvt_pk_bf16_f32 v86, v56, v57
	v_cvt_pk_bf16_f32 v87, v58, v59
	s_nop 1
	v_permlane16_swap_b32_e32 v84, v86
	v_permlane16_swap_b32_e32 v85, v87
	s_nop 1
	global_store_dwordx4 v70, v[84:87], s[58:59] offset:192
	v_mul_f32_e32 v4, v4, v67
	v_mul_f32_e32 v5, v5, v67
	v_mul_f32_e32 v6, v6, v67
	v_mul_f32_e32 v7, v7, v67
	v_mul_f32_e32 v12, v12, v67
	v_mul_f32_e32 v13, v13, v67
	v_mul_f32_e32 v14, v14, v67
	v_mul_f32_e32 v15, v15, v67
	v_cvt_pk_bf16_f32 v88, v4, v5
	v_cvt_pk_bf16_f32 v89, v6, v7
	v_cvt_pk_bf16_f32 v90, v12, v13
	v_cvt_pk_bf16_f32 v91, v14, v15
	s_nop 1
	v_permlane16_swap_b32_e32 v88, v90
	v_permlane16_swap_b32_e32 v89, v91
	s_nop 1
	global_store_dwordx4 v71, v[88:91], s[58:59] offset:0
	v_mul_f32_e32 v20, v20, v67
	v_mul_f32_e32 v21, v21, v67
	v_mul_f32_e32 v22, v22, v67
	v_mul_f32_e32 v23, v23, v67
	v_mul_f32_e32 v28, v28, v67
	v_mul_f32_e32 v29, v29, v67
	v_mul_f32_e32 v30, v30, v67
	v_mul_f32_e32 v31, v31, v67
	v_cvt_pk_bf16_f32 v92, v20, v21
	v_cvt_pk_bf16_f32 v93, v22, v23
	v_cvt_pk_bf16_f32 v94, v28, v29
	v_cvt_pk_bf16_f32 v95, v30, v31
	s_nop 1
	v_permlane16_swap_b32_e32 v92, v94
	v_permlane16_swap_b32_e32 v93, v95
	s_nop 1
	global_store_dwordx4 v71, v[92:95], s[58:59] offset:64
	v_mul_f32_e32 v36, v36, v67
	v_mul_f32_e32 v37, v37, v67
	v_mul_f32_e32 v38, v38, v67
	v_mul_f32_e32 v39, v39, v67
	v_mul_f32_e32 v44, v44, v67
	v_mul_f32_e32 v45, v45, v67
	v_mul_f32_e32 v46, v46, v67
	v_mul_f32_e32 v47, v47, v67
	v_cvt_pk_bf16_f32 v72, v36, v37
	v_cvt_pk_bf16_f32 v73, v38, v39
	v_cvt_pk_bf16_f32 v74, v44, v45
	v_cvt_pk_bf16_f32 v75, v46, v47
	s_nop 1
	v_permlane16_swap_b32_e32 v72, v74
	v_permlane16_swap_b32_e32 v73, v75
	s_nop 1
	global_store_dwordx4 v71, v[72:75], s[58:59] offset:128
	v_mul_f32_e32 v52, v52, v67
	v_mul_f32_e32 v53, v53, v67
	v_mul_f32_e32 v54, v54, v67
	v_mul_f32_e32 v55, v55, v67
	v_mul_f32_e32 v60, v60, v67
	v_mul_f32_e32 v61, v61, v67
	v_mul_f32_e32 v62, v62, v67
	v_mul_f32_e32 v63, v63, v67
	v_cvt_pk_bf16_f32 v76, v52, v53
	v_cvt_pk_bf16_f32 v77, v54, v55
	v_cvt_pk_bf16_f32 v78, v60, v61
	v_cvt_pk_bf16_f32 v79, v62, v63
	s_nop 1
	v_permlane16_swap_b32_e32 v76, v78
	v_permlane16_swap_b32_e32 v77, v79
	s_nop 1
	global_store_dwordx4 v71, v[76:79], s[58:59] offset:192
	s_barrier
